# write-through (sc1) epilogue stores in both in-projection GEMMs, so the release fence of the following grid barrier finds less dirty L2
# speedup vs baseline: 1.0037x; 1.0037x over previous
.LBB0_153:
	v_cvt_pk_bf16_f32 v114, v130, v131
	v_cvt_pk_bf16_f32 v115, v132, v133
	s_lshl_b32 s4, s4, 8
	v_cvt_pk_bf16_f32 v116, v134, v135
	s_ashr_i32 s5, s4, 31
	v_lshl_add_u32 v168, s54, 8, v164
	v_lshl_add_u64 v[162:163], s[4:5], 1, v[154:155]
	v_mad_i64_i32 v[118:119], s[4:5], v168, s86, v[162:163]
	v_cvt_pk_bf16_f32 v117, v136, v137
	global_store_dwordx4 v[118:119], v[114:117], off sc1
	s_nop 1
	v_cvt_pk_bf16_f32 v114, v138, v139
	v_cvt_pk_bf16_f32 v115, v140, v141
	v_cvt_pk_bf16_f32 v116, v142, v143
	v_cvt_pk_bf16_f32 v117, v144, v145
	global_store_dwordx4 v[118:119], v[114:117], off offset:256 sc1
	s_andn2_b64 vcc, exec, s[62:63]
	s_mov_b64 s[38:39], -1
	v_cndmask_b32_e64 v114, 0, 1, s[62:63]
	v_cmp_ne_u32_e64 s[4:5], 1, v114
	s_cbranch_vccnz .LBB0_157
	v_mov_b64_e32 v[116:117], v[112:113]
	v_mov_b64_e32 v[128:129], v[100:101]
	v_mov_b64_e32 v[124:125], v[104:105]
	v_mov_b64_e32 v[120:121], v[108:109]
	s_and_b64 vcc, exec, s[2:3]
	v_mov_b64_e32 v[114:115], v[110:111]
	v_mov_b64_e32 v[126:127], v[98:99]
	v_mov_b64_e32 v[122:123], v[102:103]
	v_mov_b64_e32 v[118:119], v[106:107]
	s_cbranch_vccnz .LBB0_156
	v_pk_mul_f32 v[116:117], v[112:113], s[24:25] op_sel_hi:[1,0]
	v_pk_mul_f32 v[114:115], v[110:111], s[24:25] op_sel_hi:[1,0]
	v_pk_mul_f32 v[120:121], v[108:109], s[24:25] op_sel_hi:[1,0]
	v_pk_mul_f32 v[118:119], v[106:107], s[24:25] op_sel_hi:[1,0]
	v_pk_mul_f32 v[124:125], v[104:105], s[24:25] op_sel_hi:[1,0]
	v_pk_mul_f32 v[122:123], v[102:103], s[24:25] op_sel_hi:[1,0]
	v_pk_mul_f32 v[128:129], v[100:101], s[24:25] op_sel_hi:[1,0]
	v_pk_mul_f32 v[126:127], v[98:99], s[24:25] op_sel_hi:[1,0]

.LBB0_159:
	v_or_b32_e32 v98, 16, v168
	v_mad_i64_i32 v[102:103], s[38:39], v98, s86, v[162:163]
	v_cvt_pk_bf16_f32 v98, v114, v115
	v_cvt_pk_bf16_f32 v99, v116, v117
	v_cvt_pk_bf16_f32 v100, v118, v119
	v_cvt_pk_bf16_f32 v101, v120, v121
	global_store_dwordx4 v[102:103], v[98:101], off sc1
	s_nop 1
	v_cvt_pk_bf16_f32 v98, v122, v123
	v_cvt_pk_bf16_f32 v99, v124, v125
	v_cvt_pk_bf16_f32 v100, v126, v127
	v_cvt_pk_bf16_f32 v101, v128, v129
	s_and_b64 vcc, exec, s[4:5]
	s_mov_b64 s[38:39], -1
	global_store_dwordx4 v[102:103], v[98:101], off offset:256 sc1
	s_cbranch_vccnz .LBB0_163
	s_nop 0
	v_mov_b64_e32 v[100:101], v[96:97]
	v_mov_b64_e32 v[112:113], v[84:85]
	v_mov_b64_e32 v[108:109], v[88:89]
	v_mov_b64_e32 v[104:105], v[92:93]
	s_and_b64 vcc, exec, s[2:3]
	v_mov_b64_e32 v[98:99], v[94:95]
	v_mov_b64_e32 v[110:111], v[82:83]
	v_mov_b64_e32 v[106:107], v[86:87]
	v_mov_b64_e32 v[102:103], v[90:91]
	s_cbranch_vccnz .LBB0_162
	v_pk_mul_f32 v[100:101], v[96:97], s[24:25] op_sel_hi:[1,0]
	v_pk_mul_f32 v[98:99], v[94:95], s[24:25] op_sel_hi:[1,0]
	v_pk_mul_f32 v[104:105], v[92:93], s[24:25] op_sel_hi:[1,0]
	v_pk_mul_f32 v[102:103], v[90:91], s[24:25] op_sel_hi:[1,0]
	v_pk_mul_f32 v[108:109], v[88:89], s[24:25] op_sel_hi:[1,0]
	v_pk_mul_f32 v[106:107], v[86:87], s[24:25] op_sel_hi:[1,0]
	v_pk_mul_f32 v[112:113], v[84:85], s[24:25] op_sel_hi:[1,0]
	v_pk_mul_f32 v[110:111], v[82:83], s[24:25] op_sel_hi:[1,0]

.LBB0_165:
	v_or_b32_e32 v82, 32, v168
	v_mad_i64_i32 v[86:87], s[38:39], v82, s86, v[162:163]
	v_cvt_pk_bf16_f32 v82, v98, v99
	v_cvt_pk_bf16_f32 v83, v100, v101
	v_cvt_pk_bf16_f32 v84, v102, v103
	v_cvt_pk_bf16_f32 v85, v104, v105
	global_store_dwordx4 v[86:87], v[82:85], off sc1
	s_nop 1
	v_cvt_pk_bf16_f32 v82, v106, v107
	v_cvt_pk_bf16_f32 v83, v108, v109
	v_cvt_pk_bf16_f32 v84, v110, v111
	v_cvt_pk_bf16_f32 v85, v112, v113
	s_and_b64 vcc, exec, s[4:5]
	s_mov_b64 s[38:39], -1
	global_store_dwordx4 v[86:87], v[82:85], off offset:256 sc1
	s_cbranch_vccnz .LBB0_169
	s_nop 0
	v_mov_b64_e32 v[84:85], v[80:81]
	v_mov_b64_e32 v[96:97], v[68:69]
	v_mov_b64_e32 v[92:93], v[72:73]
	v_mov_b64_e32 v[88:89], v[76:77]
	s_and_b64 vcc, exec, s[2:3]
	v_mov_b64_e32 v[82:83], v[78:79]
	v_mov_b64_e32 v[94:95], v[66:67]
	v_mov_b64_e32 v[90:91], v[70:71]
	v_mov_b64_e32 v[86:87], v[74:75]
	s_cbranch_vccnz .LBB0_168
	v_pk_mul_f32 v[84:85], v[80:81], s[24:25] op_sel_hi:[1,0]
	v_pk_mul_f32 v[82:83], v[78:79], s[24:25] op_sel_hi:[1,0]
	v_pk_mul_f32 v[88:89], v[76:77], s[24:25] op_sel_hi:[1,0]
	v_pk_mul_f32 v[86:87], v[74:75], s[24:25] op_sel_hi:[1,0]
	v_pk_mul_f32 v[92:93], v[72:73], s[24:25] op_sel_hi:[1,0]
	v_pk_mul_f32 v[90:91], v[70:71], s[24:25] op_sel_hi:[1,0]
	v_pk_mul_f32 v[96:97], v[68:69], s[24:25] op_sel_hi:[1,0]
	v_pk_mul_f32 v[94:95], v[66:67], s[24:25] op_sel_hi:[1,0]

.LBB0_171:
	v_or_b32_e32 v66, 48, v168
	v_mad_i64_i32 v[70:71], s[38:39], v66, s86, v[162:163]
	v_cvt_pk_bf16_f32 v66, v82, v83
	v_cvt_pk_bf16_f32 v67, v84, v85
	v_cvt_pk_bf16_f32 v68, v86, v87
	v_cvt_pk_bf16_f32 v69, v88, v89
	global_store_dwordx4 v[70:71], v[66:69], off sc1
	s_nop 1
	v_cvt_pk_bf16_f32 v66, v90, v91
	v_cvt_pk_bf16_f32 v67, v92, v93
	v_cvt_pk_bf16_f32 v68, v94, v95
	v_cvt_pk_bf16_f32 v69, v96, v97
	s_and_b64 vcc, exec, s[4:5]
	s_mov_b64 s[38:39], -1
	global_store_dwordx4 v[70:71], v[66:69], off offset:256 sc1
	s_cbranch_vccnz .LBB0_175
	s_nop 0
	v_mov_b64_e32 v[68:69], v[64:65]
	v_mov_b64_e32 v[80:81], v[52:53]
	v_mov_b64_e32 v[76:77], v[56:57]
	v_mov_b64_e32 v[72:73], v[60:61]
	s_and_b64 vcc, exec, s[2:3]
	v_mov_b64_e32 v[66:67], v[62:63]
	v_mov_b64_e32 v[78:79], v[50:51]
	v_mov_b64_e32 v[74:75], v[54:55]
	v_mov_b64_e32 v[70:71], v[58:59]
	s_cbranch_vccnz .LBB0_174
	v_pk_mul_f32 v[68:69], v[64:65], s[24:25] op_sel_hi:[1,0]
	v_pk_mul_f32 v[66:67], v[62:63], s[24:25] op_sel_hi:[1,0]
	v_pk_mul_f32 v[72:73], v[60:61], s[24:25] op_sel_hi:[1,0]
	v_pk_mul_f32 v[70:71], v[58:59], s[24:25] op_sel_hi:[1,0]
	v_pk_mul_f32 v[76:77], v[56:57], s[24:25] op_sel_hi:[1,0]
	v_pk_mul_f32 v[74:75], v[54:55], s[24:25] op_sel_hi:[1,0]
	v_pk_mul_f32 v[80:81], v[52:53], s[24:25] op_sel_hi:[1,0]
	v_pk_mul_f32 v[78:79], v[50:51], s[24:25] op_sel_hi:[1,0]

.LBB0_177:
	v_add_u32_e32 v50, 0x80, v168
	v_mad_i64_i32 v[54:55], s[38:39], v50, s86, v[162:163]
	v_cvt_pk_bf16_f32 v50, v66, v67
	v_cvt_pk_bf16_f32 v51, v68, v69
	v_cvt_pk_bf16_f32 v52, v70, v71
	v_cvt_pk_bf16_f32 v53, v72, v73
	global_store_dwordx4 v[54:55], v[50:53], off sc1
	s_nop 1
	v_cvt_pk_bf16_f32 v50, v74, v75
	v_cvt_pk_bf16_f32 v51, v76, v77
	v_cvt_pk_bf16_f32 v52, v78, v79
	v_cvt_pk_bf16_f32 v53, v80, v81
	s_and_b64 vcc, exec, s[4:5]
	s_mov_b64 s[38:39], -1
	global_store_dwordx4 v[54:55], v[50:53], off offset:256 sc1
	s_cbranch_vccnz .LBB0_181
	s_nop 0
	v_mov_b64_e32 v[52:53], v[48:49]
	v_mov_b64_e32 v[64:65], v[36:37]
	v_mov_b64_e32 v[60:61], v[40:41]
	v_mov_b64_e32 v[56:57], v[44:45]
	s_and_b64 vcc, exec, s[2:3]
	v_mov_b64_e32 v[50:51], v[46:47]
	v_mov_b64_e32 v[62:63], v[34:35]
	v_mov_b64_e32 v[58:59], v[38:39]
	v_mov_b64_e32 v[54:55], v[42:43]
	s_cbranch_vccnz .LBB0_180
	v_pk_mul_f32 v[52:53], v[48:49], s[24:25] op_sel_hi:[1,0]
	v_pk_mul_f32 v[50:51], v[46:47], s[24:25] op_sel_hi:[1,0]
	v_pk_mul_f32 v[56:57], v[44:45], s[24:25] op_sel_hi:[1,0]
	v_pk_mul_f32 v[54:55], v[42:43], s[24:25] op_sel_hi:[1,0]
	v_pk_mul_f32 v[60:61], v[40:41], s[24:25] op_sel_hi:[1,0]
	v_pk_mul_f32 v[58:59], v[38:39], s[24:25] op_sel_hi:[1,0]
	v_pk_mul_f32 v[64:65], v[36:37], s[24:25] op_sel_hi:[1,0]
	v_pk_mul_f32 v[62:63], v[34:35], s[24:25] op_sel_hi:[1,0]

.LBB0_183:
	v_add_u32_e32 v34, 0x90, v168
	v_mad_i64_i32 v[38:39], s[38:39], v34, s86, v[162:163]
	v_cvt_pk_bf16_f32 v34, v50, v51
	v_cvt_pk_bf16_f32 v35, v52, v53
	v_cvt_pk_bf16_f32 v36, v54, v55
	v_cvt_pk_bf16_f32 v37, v56, v57
	global_store_dwordx4 v[38:39], v[34:37], off sc1
	s_nop 1
	v_cvt_pk_bf16_f32 v34, v58, v59
	v_cvt_pk_bf16_f32 v35, v60, v61
	v_cvt_pk_bf16_f32 v36, v62, v63
	v_cvt_pk_bf16_f32 v37, v64, v65
	s_and_b64 vcc, exec, s[4:5]
	s_mov_b64 s[38:39], -1
	global_store_dwordx4 v[38:39], v[34:37], off offset:256 sc1
	s_cbranch_vccnz .LBB0_187
	s_nop 0
	v_mov_b64_e32 v[36:37], v[32:33]
	v_mov_b64_e32 v[48:49], v[20:21]
	v_mov_b64_e32 v[44:45], v[24:25]
	v_mov_b64_e32 v[40:41], v[28:29]
	s_and_b64 vcc, exec, s[2:3]
	v_mov_b64_e32 v[34:35], v[30:31]
	v_mov_b64_e32 v[46:47], v[18:19]
	v_mov_b64_e32 v[42:43], v[22:23]
	v_mov_b64_e32 v[38:39], v[26:27]
	s_cbranch_vccnz .LBB0_186
	v_pk_mul_f32 v[36:37], v[32:33], s[24:25] op_sel_hi:[1,0]
	v_pk_mul_f32 v[34:35], v[30:31], s[24:25] op_sel_hi:[1,0]
	v_pk_mul_f32 v[40:41], v[28:29], s[24:25] op_sel_hi:[1,0]
	v_pk_mul_f32 v[38:39], v[26:27], s[24:25] op_sel_hi:[1,0]
	v_pk_mul_f32 v[44:45], v[24:25], s[24:25] op_sel_hi:[1,0]
	v_pk_mul_f32 v[42:43], v[22:23], s[24:25] op_sel_hi:[1,0]
	v_pk_mul_f32 v[48:49], v[20:21], s[24:25] op_sel_hi:[1,0]
	v_pk_mul_f32 v[46:47], v[18:19], s[24:25] op_sel_hi:[1,0]

.LBB0_189:
	v_add_u32_e32 v18, 0xa0, v168
	v_mad_i64_i32 v[22:23], s[38:39], v18, s86, v[162:163]
	v_cvt_pk_bf16_f32 v18, v34, v35
	v_cvt_pk_bf16_f32 v19, v36, v37
	v_cvt_pk_bf16_f32 v20, v38, v39
	v_cvt_pk_bf16_f32 v21, v40, v41
	global_store_dwordx4 v[22:23], v[18:21], off sc1
	s_nop 1
	v_cvt_pk_bf16_f32 v18, v42, v43
	v_cvt_pk_bf16_f32 v19, v44, v45
	v_cvt_pk_bf16_f32 v20, v46, v47
	v_cvt_pk_bf16_f32 v21, v48, v49
	s_and_b64 vcc, exec, s[4:5]
	s_mov_b64 s[4:5], -1
	global_store_dwordx4 v[22:23], v[18:21], off offset:256 sc1
	s_cbranch_vccnz .LBB0_193
	s_nop 0
	v_mov_b64_e32 v[20:21], v[16:17]
	v_mov_b64_e32 v[32:33], v[4:5]
	v_mov_b64_e32 v[28:29], v[8:9]
	v_mov_b64_e32 v[24:25], v[12:13]
	s_and_b64 vcc, exec, s[2:3]
	v_mov_b64_e32 v[18:19], v[14:15]
	v_mov_b64_e32 v[30:31], v[2:3]
	v_mov_b64_e32 v[26:27], v[6:7]
	v_mov_b64_e32 v[22:23], v[10:11]
	s_cbranch_vccnz .LBB0_192
	v_pk_mul_f32 v[20:21], v[16:17], s[24:25] op_sel_hi:[1,0]
	v_pk_mul_f32 v[18:19], v[14:15], s[24:25] op_sel_hi:[1,0]
	v_pk_mul_f32 v[24:25], v[12:13], s[24:25] op_sel_hi:[1,0]
	v_pk_mul_f32 v[22:23], v[10:11], s[24:25] op_sel_hi:[1,0]
	v_pk_mul_f32 v[28:29], v[8:9], s[24:25] op_sel_hi:[1,0]
	v_pk_mul_f32 v[26:27], v[6:7], s[24:25] op_sel_hi:[1,0]
	v_pk_mul_f32 v[32:33], v[4:5], s[24:25] op_sel_hi:[1,0]
	v_pk_mul_f32 v[30:31], v[2:3], s[24:25] op_sel_hi:[1,0]

.LBB0_195:
	v_add_u32_e32 v2, 0xb0, v168
	v_mad_i64_i32 v[6:7], s[2:3], v2, s86, v[162:163]
	v_cvt_pk_bf16_f32 v2, v18, v19
	v_cvt_pk_bf16_f32 v3, v20, v21
	v_cvt_pk_bf16_f32 v4, v22, v23
	v_cvt_pk_bf16_f32 v5, v24, v25
	global_store_dwordx4 v[6:7], v[2:5], off sc1
	s_nop 1
	v_cvt_pk_bf16_f32 v2, v26, v27
	v_cvt_pk_bf16_f32 v3, v28, v29
	v_cvt_pk_bf16_f32 v4, v30, v31
	v_cvt_pk_bf16_f32 v5, v32, v33
	s_mov_b64 s[2:3], -1
	s_and_b64 vcc, exec, s[46:47]
	global_store_dwordx4 v[6:7], v[2:5], off offset:256 sc1
	s_cbranch_vccz .LBB0_139
	s_and_b64 vcc, exec, s[6:7]
	s_cbranch_vccz .LBB0_138
	s_barrier
	s_branch .LBB0_138

.LBB0_767:
	v_cvt_pk_bf16_f32 v114, v130, v131
	v_cvt_pk_bf16_f32 v115, v132, v133
	s_lshl_b32 s4, s72, 8
	v_cvt_pk_bf16_f32 v116, v134, v135
	s_ashr_i32 s5, s4, 31
	v_lshl_add_u32 v166, s73, 8, v162
	v_lshl_add_u64 v[160:161], s[4:5], 1, v[154:155]
	v_mad_i64_i32 v[118:119], s[4:5], v166, s77, v[160:161]
	v_cvt_pk_bf16_f32 v117, v136, v137
	global_store_dwordx4 v[118:119], v[114:117], off sc1
	s_nop 1
	v_cvt_pk_bf16_f32 v114, v138, v139
	v_cvt_pk_bf16_f32 v115, v140, v141
	v_cvt_pk_bf16_f32 v116, v142, v143
	v_cvt_pk_bf16_f32 v117, v144, v145
	global_store_dwordx4 v[118:119], v[114:117], off offset:256 sc1
	s_andn2_b64 vcc, exec, s[52:53]
	s_mov_b64 s[38:39], -1
	v_cndmask_b32_e64 v114, 0, 1, s[52:53]
	v_cmp_ne_u32_e64 s[4:5], 1, v114
	s_cbranch_vccnz .LBB0_771
	v_mov_b64_e32 v[116:117], v[112:113]
	v_mov_b64_e32 v[128:129], v[100:101]
	v_mov_b64_e32 v[124:125], v[104:105]
	v_mov_b64_e32 v[120:121], v[108:109]
	s_and_b64 vcc, exec, s[2:3]
	v_mov_b64_e32 v[114:115], v[110:111]
	v_mov_b64_e32 v[126:127], v[98:99]
	v_mov_b64_e32 v[122:123], v[102:103]
	v_mov_b64_e32 v[118:119], v[106:107]
	s_cbranch_vccnz .LBB0_770
	v_pk_mul_f32 v[116:117], v[112:113], s[20:21] op_sel_hi:[1,0]
	v_pk_mul_f32 v[114:115], v[110:111], s[20:21] op_sel_hi:[1,0]
	v_pk_mul_f32 v[120:121], v[108:109], s[20:21] op_sel_hi:[1,0]
	v_pk_mul_f32 v[118:119], v[106:107], s[20:21] op_sel_hi:[1,0]
	v_pk_mul_f32 v[124:125], v[104:105], s[20:21] op_sel_hi:[1,0]
	v_pk_mul_f32 v[122:123], v[102:103], s[20:21] op_sel_hi:[1,0]
	v_pk_mul_f32 v[128:129], v[100:101], s[20:21] op_sel_hi:[1,0]
	v_pk_mul_f32 v[126:127], v[98:99], s[20:21] op_sel_hi:[1,0]

.LBB0_773:
	v_or_b32_e32 v98, 16, v166
	v_mad_i64_i32 v[102:103], s[38:39], v98, s77, v[160:161]
	v_cvt_pk_bf16_f32 v98, v114, v115
	v_cvt_pk_bf16_f32 v99, v116, v117
	v_cvt_pk_bf16_f32 v100, v118, v119
	v_cvt_pk_bf16_f32 v101, v120, v121
	global_store_dwordx4 v[102:103], v[98:101], off sc1
	s_nop 1
	v_cvt_pk_bf16_f32 v98, v122, v123
	v_cvt_pk_bf16_f32 v99, v124, v125
	v_cvt_pk_bf16_f32 v100, v126, v127
	v_cvt_pk_bf16_f32 v101, v128, v129
	s_and_b64 vcc, exec, s[4:5]
	s_mov_b64 s[38:39], -1
	global_store_dwordx4 v[102:103], v[98:101], off offset:256 sc1
	s_cbranch_vccnz .LBB0_777
	s_nop 0
	v_mov_b64_e32 v[100:101], v[96:97]
	v_mov_b64_e32 v[112:113], v[84:85]
	v_mov_b64_e32 v[108:109], v[88:89]
	v_mov_b64_e32 v[104:105], v[92:93]
	s_and_b64 vcc, exec, s[2:3]
	v_mov_b64_e32 v[98:99], v[94:95]
	v_mov_b64_e32 v[110:111], v[82:83]
	v_mov_b64_e32 v[106:107], v[86:87]
	v_mov_b64_e32 v[102:103], v[90:91]
	s_cbranch_vccnz .LBB0_776
	v_pk_mul_f32 v[100:101], v[96:97], s[20:21] op_sel_hi:[1,0]
	v_pk_mul_f32 v[98:99], v[94:95], s[20:21] op_sel_hi:[1,0]
	v_pk_mul_f32 v[104:105], v[92:93], s[20:21] op_sel_hi:[1,0]
	v_pk_mul_f32 v[102:103], v[90:91], s[20:21] op_sel_hi:[1,0]
	v_pk_mul_f32 v[108:109], v[88:89], s[20:21] op_sel_hi:[1,0]
	v_pk_mul_f32 v[106:107], v[86:87], s[20:21] op_sel_hi:[1,0]
	v_pk_mul_f32 v[112:113], v[84:85], s[20:21] op_sel_hi:[1,0]
	v_pk_mul_f32 v[110:111], v[82:83], s[20:21] op_sel_hi:[1,0]

.LBB0_779:
	v_or_b32_e32 v82, 32, v166
	v_mad_i64_i32 v[86:87], s[38:39], v82, s77, v[160:161]
	v_cvt_pk_bf16_f32 v82, v98, v99
	v_cvt_pk_bf16_f32 v83, v100, v101
	v_cvt_pk_bf16_f32 v84, v102, v103
	v_cvt_pk_bf16_f32 v85, v104, v105
	global_store_dwordx4 v[86:87], v[82:85], off sc1
	s_nop 1
	v_cvt_pk_bf16_f32 v82, v106, v107
	v_cvt_pk_bf16_f32 v83, v108, v109
	v_cvt_pk_bf16_f32 v84, v110, v111
	v_cvt_pk_bf16_f32 v85, v112, v113
	s_and_b64 vcc, exec, s[4:5]
	s_mov_b64 s[38:39], -1
	global_store_dwordx4 v[86:87], v[82:85], off offset:256 sc1
	s_cbranch_vccnz .LBB0_783
	s_nop 0
	v_mov_b64_e32 v[84:85], v[80:81]
	v_mov_b64_e32 v[96:97], v[68:69]
	v_mov_b64_e32 v[92:93], v[72:73]
	v_mov_b64_e32 v[88:89], v[76:77]
	s_and_b64 vcc, exec, s[2:3]
	v_mov_b64_e32 v[82:83], v[78:79]
	v_mov_b64_e32 v[94:95], v[66:67]
	v_mov_b64_e32 v[90:91], v[70:71]
	v_mov_b64_e32 v[86:87], v[74:75]
	s_cbranch_vccnz .LBB0_782
	v_pk_mul_f32 v[84:85], v[80:81], s[20:21] op_sel_hi:[1,0]
	v_pk_mul_f32 v[82:83], v[78:79], s[20:21] op_sel_hi:[1,0]
	v_pk_mul_f32 v[88:89], v[76:77], s[20:21] op_sel_hi:[1,0]
	v_pk_mul_f32 v[86:87], v[74:75], s[20:21] op_sel_hi:[1,0]
	v_pk_mul_f32 v[92:93], v[72:73], s[20:21] op_sel_hi:[1,0]
	v_pk_mul_f32 v[90:91], v[70:71], s[20:21] op_sel_hi:[1,0]
	v_pk_mul_f32 v[96:97], v[68:69], s[20:21] op_sel_hi:[1,0]
	v_pk_mul_f32 v[94:95], v[66:67], s[20:21] op_sel_hi:[1,0]

.LBB0_785:
	v_or_b32_e32 v66, 48, v166
	v_mad_i64_i32 v[70:71], s[38:39], v66, s77, v[160:161]
	v_cvt_pk_bf16_f32 v66, v82, v83
	v_cvt_pk_bf16_f32 v67, v84, v85
	v_cvt_pk_bf16_f32 v68, v86, v87
	v_cvt_pk_bf16_f32 v69, v88, v89
	global_store_dwordx4 v[70:71], v[66:69], off sc1
	s_nop 1
	v_cvt_pk_bf16_f32 v66, v90, v91
	v_cvt_pk_bf16_f32 v67, v92, v93
	v_cvt_pk_bf16_f32 v68, v94, v95
	v_cvt_pk_bf16_f32 v69, v96, v97
	s_and_b64 vcc, exec, s[4:5]
	s_mov_b64 s[38:39], -1
	global_store_dwordx4 v[70:71], v[66:69], off offset:256 sc1
	s_cbranch_vccnz .LBB0_789
	s_nop 0
	v_mov_b64_e32 v[68:69], v[64:65]
	v_mov_b64_e32 v[80:81], v[52:53]
	v_mov_b64_e32 v[76:77], v[56:57]
	v_mov_b64_e32 v[72:73], v[60:61]
	s_and_b64 vcc, exec, s[2:3]
	v_mov_b64_e32 v[66:67], v[62:63]
	v_mov_b64_e32 v[78:79], v[50:51]
	v_mov_b64_e32 v[74:75], v[54:55]
	v_mov_b64_e32 v[70:71], v[58:59]
	s_cbranch_vccnz .LBB0_788
	v_pk_mul_f32 v[68:69], v[64:65], s[20:21] op_sel_hi:[1,0]
	v_pk_mul_f32 v[66:67], v[62:63], s[20:21] op_sel_hi:[1,0]
	v_pk_mul_f32 v[72:73], v[60:61], s[20:21] op_sel_hi:[1,0]
	v_pk_mul_f32 v[70:71], v[58:59], s[20:21] op_sel_hi:[1,0]
	v_pk_mul_f32 v[76:77], v[56:57], s[20:21] op_sel_hi:[1,0]
	v_pk_mul_f32 v[74:75], v[54:55], s[20:21] op_sel_hi:[1,0]
	v_pk_mul_f32 v[80:81], v[52:53], s[20:21] op_sel_hi:[1,0]
	v_pk_mul_f32 v[78:79], v[50:51], s[20:21] op_sel_hi:[1,0]

.LBB0_791:
	v_add_u32_e32 v50, 0x80, v166
	v_mad_i64_i32 v[54:55], s[38:39], v50, s77, v[160:161]
	v_cvt_pk_bf16_f32 v50, v66, v67
	v_cvt_pk_bf16_f32 v51, v68, v69
	v_cvt_pk_bf16_f32 v52, v70, v71
	v_cvt_pk_bf16_f32 v53, v72, v73
	global_store_dwordx4 v[54:55], v[50:53], off sc1
	s_nop 1
	v_cvt_pk_bf16_f32 v50, v74, v75
	v_cvt_pk_bf16_f32 v51, v76, v77
	v_cvt_pk_bf16_f32 v52, v78, v79
	v_cvt_pk_bf16_f32 v53, v80, v81
	s_and_b64 vcc, exec, s[4:5]
	s_mov_b64 s[38:39], -1
	global_store_dwordx4 v[54:55], v[50:53], off offset:256 sc1
	s_cbranch_vccnz .LBB0_795
	s_nop 0
	v_mov_b64_e32 v[52:53], v[48:49]
	v_mov_b64_e32 v[64:65], v[36:37]
	v_mov_b64_e32 v[60:61], v[40:41]
	v_mov_b64_e32 v[56:57], v[44:45]
	s_and_b64 vcc, exec, s[2:3]
	v_mov_b64_e32 v[50:51], v[46:47]
	v_mov_b64_e32 v[62:63], v[34:35]
	v_mov_b64_e32 v[58:59], v[38:39]
	v_mov_b64_e32 v[54:55], v[42:43]
	s_cbranch_vccnz .LBB0_794
	v_pk_mul_f32 v[52:53], v[48:49], s[20:21] op_sel_hi:[1,0]
	v_pk_mul_f32 v[50:51], v[46:47], s[20:21] op_sel_hi:[1,0]
	v_pk_mul_f32 v[56:57], v[44:45], s[20:21] op_sel_hi:[1,0]
	v_pk_mul_f32 v[54:55], v[42:43], s[20:21] op_sel_hi:[1,0]
	v_pk_mul_f32 v[60:61], v[40:41], s[20:21] op_sel_hi:[1,0]
	v_pk_mul_f32 v[58:59], v[38:39], s[20:21] op_sel_hi:[1,0]
	v_pk_mul_f32 v[64:65], v[36:37], s[20:21] op_sel_hi:[1,0]
	v_pk_mul_f32 v[62:63], v[34:35], s[20:21] op_sel_hi:[1,0]

.LBB0_797:
	v_add_u32_e32 v34, 0x90, v166
	v_mad_i64_i32 v[38:39], s[38:39], v34, s77, v[160:161]
	v_cvt_pk_bf16_f32 v34, v50, v51
	v_cvt_pk_bf16_f32 v35, v52, v53
	v_cvt_pk_bf16_f32 v36, v54, v55
	v_cvt_pk_bf16_f32 v37, v56, v57
	global_store_dwordx4 v[38:39], v[34:37], off sc1
	s_nop 1
	v_cvt_pk_bf16_f32 v34, v58, v59
	v_cvt_pk_bf16_f32 v35, v60, v61
	v_cvt_pk_bf16_f32 v36, v62, v63
	v_cvt_pk_bf16_f32 v37, v64, v65
	s_and_b64 vcc, exec, s[4:5]
	s_mov_b64 s[38:39], -1
	global_store_dwordx4 v[38:39], v[34:37], off offset:256 sc1
	s_cbranch_vccnz .LBB0_801
	s_nop 0
	v_mov_b64_e32 v[36:37], v[32:33]
	v_mov_b64_e32 v[48:49], v[20:21]
	v_mov_b64_e32 v[44:45], v[24:25]
	v_mov_b64_e32 v[40:41], v[28:29]
	s_and_b64 vcc, exec, s[2:3]
	v_mov_b64_e32 v[34:35], v[30:31]
	v_mov_b64_e32 v[46:47], v[18:19]
	v_mov_b64_e32 v[42:43], v[22:23]
	v_mov_b64_e32 v[38:39], v[26:27]
	s_cbranch_vccnz .LBB0_800
	v_pk_mul_f32 v[36:37], v[32:33], s[20:21] op_sel_hi:[1,0]
	v_pk_mul_f32 v[34:35], v[30:31], s[20:21] op_sel_hi:[1,0]
	v_pk_mul_f32 v[40:41], v[28:29], s[20:21] op_sel_hi:[1,0]
	v_pk_mul_f32 v[38:39], v[26:27], s[20:21] op_sel_hi:[1,0]
	v_pk_mul_f32 v[44:45], v[24:25], s[20:21] op_sel_hi:[1,0]
	v_pk_mul_f32 v[42:43], v[22:23], s[20:21] op_sel_hi:[1,0]
	v_pk_mul_f32 v[48:49], v[20:21], s[20:21] op_sel_hi:[1,0]
	v_pk_mul_f32 v[46:47], v[18:19], s[20:21] op_sel_hi:[1,0]

.LBB0_803:
	v_add_u32_e32 v18, 0xa0, v166
	v_mad_i64_i32 v[22:23], s[38:39], v18, s77, v[160:161]
	v_cvt_pk_bf16_f32 v18, v34, v35
	v_cvt_pk_bf16_f32 v19, v36, v37
	v_cvt_pk_bf16_f32 v20, v38, v39
	v_cvt_pk_bf16_f32 v21, v40, v41
	global_store_dwordx4 v[22:23], v[18:21], off sc1
	s_nop 1
	v_cvt_pk_bf16_f32 v18, v42, v43
	v_cvt_pk_bf16_f32 v19, v44, v45
	v_cvt_pk_bf16_f32 v20, v46, v47
	v_cvt_pk_bf16_f32 v21, v48, v49
	s_and_b64 vcc, exec, s[4:5]
	s_mov_b64 s[4:5], -1
	global_store_dwordx4 v[22:23], v[18:21], off offset:256 sc1
	s_cbranch_vccnz .LBB0_807
	s_nop 0
	v_mov_b64_e32 v[20:21], v[16:17]
	v_mov_b64_e32 v[32:33], v[4:5]
	v_mov_b64_e32 v[28:29], v[8:9]
	v_mov_b64_e32 v[24:25], v[12:13]
	s_and_b64 vcc, exec, s[2:3]
	v_mov_b64_e32 v[18:19], v[14:15]
	v_mov_b64_e32 v[30:31], v[2:3]
	v_mov_b64_e32 v[26:27], v[6:7]
	v_mov_b64_e32 v[22:23], v[10:11]
	s_cbranch_vccnz .LBB0_806
	v_pk_mul_f32 v[20:21], v[16:17], s[20:21] op_sel_hi:[1,0]
	v_pk_mul_f32 v[18:19], v[14:15], s[20:21] op_sel_hi:[1,0]
	v_pk_mul_f32 v[24:25], v[12:13], s[20:21] op_sel_hi:[1,0]
	v_pk_mul_f32 v[22:23], v[10:11], s[20:21] op_sel_hi:[1,0]
	v_pk_mul_f32 v[28:29], v[8:9], s[20:21] op_sel_hi:[1,0]
	v_pk_mul_f32 v[26:27], v[6:7], s[20:21] op_sel_hi:[1,0]
	v_pk_mul_f32 v[32:33], v[4:5], s[20:21] op_sel_hi:[1,0]
	v_pk_mul_f32 v[30:31], v[2:3], s[20:21] op_sel_hi:[1,0]

.LBB0_809:
	v_add_u32_e32 v2, 0xb0, v166
	v_mad_i64_i32 v[6:7], s[2:3], v2, s77, v[160:161]
	v_cvt_pk_bf16_f32 v2, v18, v19
	v_cvt_pk_bf16_f32 v3, v20, v21
	v_cvt_pk_bf16_f32 v4, v22, v23
	v_cvt_pk_bf16_f32 v5, v24, v25
	global_store_dwordx4 v[6:7], v[2:5], off sc1
	s_nop 1
	v_cvt_pk_bf16_f32 v2, v26, v27
	v_cvt_pk_bf16_f32 v3, v28, v29
	v_cvt_pk_bf16_f32 v4, v30, v31
	v_cvt_pk_bf16_f32 v5, v32, v33
	s_mov_b64 s[2:3], -1
	s_and_b64 vcc, exec, s[44:45]
	global_store_dwordx4 v[6:7], v[2:5], off offset:256 sc1
	s_cbranch_vccz .LBB0_754
	s_and_b64 vcc, exec, s[6:7]
	s_cbranch_vccz .LBB0_753
	s_barrier
	s_branch .LBB0_753
